# v11 + GLA scan: the two 8-byte o stores per wave-step merged into one 16-byte store (v_permlane16_swap exchange), counted vmcnt waits re-derived
# speedup vs baseline: 1.0126x; 1.0028x over previous
.LBB0_471:
	s_or_b64 exec, exec, s[16:17]
	s_lshr_b32 s14, s56, 3
	s_lshr_b32 s15, s56, 2
	s_and_b32 s14, s14, 3
	s_mul_i32 s16, s14, 0x88
	s_and_b32 s14, s15, 1
	s_mul_i32 s17, s14, 0x44
	s_and_b64 s[14:15], s[12:13], exec
	s_cselect_b32 s14, 0, 0x4400000
	s_add_u32 s14, s22, s14
	s_addc_u32 s15, s23, 0
	s_add_u32 s14, s14, s19
	s_addc_u32 s15, s15, 0
	s_add_u32 s14, s14, s58
	s_addc_u32 s15, s15, 0
	v_lshl_add_u64 v[130:131], v[128:129], 1, s[14:15]
	v_and_b32_e32 v176, 4, v128
	v_mul_u32_u24_e32 v176, 6, v176
	v_mov_b32_e32 v177, 0
	v_lshl_add_u64 v[130:131], v[130:131], 0, v[176:177]
	s_add_u32 s14, s20, s19
	s_addc_u32 s15, s21, 0
	s_add_u32 s58, s14, s58
	s_mulk_i32 s9, 0x220
	s_addc_u32 s59, s15, 0
	s_add_i32 s60, s9, s16
	v_mov_b32_e32 v0, 0
	v_add_u32_e32 v159, s18, v135
	s_add_i32 s60, s60, s17
	s_movk_i32 s61, 0x41
	s_mov_b32 s62, 2
	v_mov_b32_e32 v1, v0
	v_mov_b32_e32 v2, v0
	v_mov_b32_e32 v3, v0
	v_mov_b32_e32 v4, v0
	v_mov_b32_e32 v5, v0
	v_mov_b32_e32 v6, v0
	v_mov_b32_e32 v7, v0
	v_mov_b32_e32 v12, v0
	v_mov_b32_e32 v13, v0
	v_mov_b32_e32 v14, v0
	v_mov_b32_e32 v15, v0
	v_mov_b32_e32 v8, v0
	v_mov_b32_e32 v9, v0
	v_mov_b32_e32 v10, v0
	v_mov_b32_e32 v11, v0
	s_waitcnt lgkmcnt(0)
	s_barrier
	s_branch .LBB0_473
.LBB0_472:
	v_mfma_f32_16x16x32_bf16 v[60:63], v[90:93], v[74:77], v[124:127]
	s_add_i32 s61, s61, -1
	s_add_i32 s62, s62, 1
	s_cmpk_eq_i32 s62, 0x46
	v_mfma_f32_16x16x32_bf16 v[56:59], v[78:81], v[74:77], v[120:123]
	v_exp_f32_e32 v74, v116
	v_exp_f32_e32 v76, v118
	v_exp_f32_e32 v77, v119
	v_mfma_f32_16x16x32_bf16 v[60:63], v[102:105], v[82:85], v[60:63]
	v_exp_f32_e32 v75, v117
	v_pk_mul_f32 v[2:3], v[2:3], v[76:77]
	v_mfma_f32_16x16x32_bf16 v[56:59], v[98:101], v[82:85], v[56:59]
	v_mul_f32_e64 v0, v0, v74
	v_mul_f32_e64 v1, v1, v75
	v_pk_mul_f32 v[6:7], v[6:7], v[76:77]
	v_pk_mul_f32 v[4:5], v[4:5], v[74:75]
	v_mfma_f32_16x16x32_bf16 v[60:63], v[106:109], v[86:89], v[60:63]
	v_mul_f32_e64 v14, v14, v76
	v_mul_f32_e64 v15, v15, v77
	v_pk_mul_f32 v[12:13], v[12:13], v[74:75]
	v_pk_mul_f32 v[10:11], v[10:11], v[76:77]
	v_mfma_f32_16x16x32_bf16 v[0:3], v[24:27], v[52:55], v[0:3]
	v_mul_f32_e64 v8, v8, v74
	v_mul_f32_e64 v9, v9, v75
	v_add_u32_e32 v52, s9, v159
	v_ashrrev_i32_e32 v53, 31, v52
	v_mfma_f32_16x16x32_bf16 v[4:7], v[24:27], v[48:51], v[4:7]
	v_lshlrev_b64 v[48:49], 11, v[52:53]
	v_lshl_add_u64 v[48:49], v[130:131], 0, v[48:49]
	s_mov_b32 s9, s31
	v_mfma_f32_16x16x32_bf16 v[56:59], v[110:113], v[86:89], v[56:59]
	v_mfma_f32_16x16x32_bf16 v[12:15], v[24:27], v[44:47], v[12:15]
	v_lshl_add_u64 v[44:45], v[48:49], 0, s[30:31]
	v_mfma_f32_16x16x32_bf16 v[8:11], v[24:27], v[40:43], v[8:11]
	s_nop 0
	v_mfma_f32_16x16x32_bf16 v[60:63], v[70:73], v[66:69], v[60:63]
	v_mfma_f32_16x16x32_bf16 v[0:3], v[16:19], v[36:39], v[0:3]
	v_mfma_f32_16x16x32_bf16 v[4:7], v[16:19], v[32:35], v[4:7]
	s_nop 5
	v_cvt_pk_bf16_f32 v182, v60, v61
	v_cvt_pk_bf16_f32 v183, v62, v63
	s_nop 0
	v_mfma_f32_16x16x32_bf16 v[56:59], v[94:97], v[66:69], v[56:59]
	v_cvt_pk_bf16_f32 v24, v0, v1
	v_cvt_pk_bf16_f32 v25, v2, v3
	v_cvt_pk_bf16_f32 v26, v4, v5
	v_mfma_f32_16x16x32_bf16 v[12:15], v[16:19], v[28:31], v[12:15]
	v_cvt_pk_bf16_f32 v27, v6, v7
	s_nop 2
	v_cvt_pk_bf16_f32 v180, v56, v57
	v_cvt_pk_bf16_f32 v181, v58, v59
	v_mfma_f32_16x16x32_bf16 v[8:11], v[16:19], v[20:23], v[8:11]
	ds_write2st64_b64 v158, v[24:25], v[26:27] offset1:8
	v_cvt_pk_bf16_f32 v24, v12, v13
	v_cvt_pk_bf16_f32 v25, v14, v15
	v_permlane16_swap_b32_e32 v180, v182
	v_permlane16_swap_b32_e32 v181, v183
	global_store_dwordx4 v[44:45], v[180:183], off
	s_nop 3
	v_cvt_pk_bf16_f32 v16, v8, v9
	v_cvt_pk_bf16_f32 v17, v10, v11
	ds_write2st64_b64 v158, v[24:25], v[16:17] offset0:16 offset1:24
	s_cbranch_scc1 .LBB0_463

.LBB0_492:
	s_cmpk_gt_i32 s63, 0x42
	s_cbranch_scc0 .LBB0_496
	s_cmpk_eq_i32 s63, 0x43
	s_mov_b64 s[16:17], -1
	s_cbranch_scc0 .LBB0_495
	s_waitcnt vmcnt(2)
	s_mov_b64 s[16:17], 0

.LBB0_496:
	s_and_b64 vcc, exec, s[18:19]
	s_cbranch_vccz .LBB0_503
	s_cmp_eq_u32 s63, 1
	s_mov_b64 s[16:17], -1
	s_cbranch_scc0 .LBB0_503
	s_and_b64 vcc, exec, s[2:3]
	s_cbranch_vccz .LBB0_500
	s_waitcnt vmcnt(7)
	s_mov_b64 s[16:17], 0
.LBB0_500:
	s_andn2_b64 vcc, exec, s[16:17]
	s_cbranch_vccnz .LBB0_502
	s_waitcnt vmcnt(8)

.LBB0_505:
	s_mov_b64 s[14:15], -1
	s_and_b64 vcc, exec, s[2:3]
	s_cbranch_vccz .LBB0_507
	s_waitcnt vmcnt(8)
	s_mov_b64 s[14:15], 0
.LBB0_507:
	s_andn2_b64 vcc, exec, s[14:15]
	s_cbranch_vccnz .LBB0_509
	s_waitcnt vmcnt(9)
